# baseline (speedup 1.0000x reference)
.LBB0_34:
	s_or_b64 exec, exec, s[10:11]
	ds_read_b128 v[18:21], v72
	s_waitcnt vmcnt(3)
	v_cvt_pk_f16_f32 v14, v14, v15
	v_cvt_pk_f16_f32 v15, v16, v17
	v_cvt_pk_f16_f32 v16, v10, v11
	ds_read_b128 v[22:25], v71 offset:41984
	v_cvt_pk_f16_f32 v17, v12, v13
	ds_read_b128 v[10:13], v72 offset:1024
	ds_read_b128 v[26:29], v71 offset:42048
	s_waitcnt vmcnt(1)
	v_cvt_pk_f16_f32 v0, v6, v7
	v_cvt_pk_f16_f32 v1, v8, v9
	v_cvt_pk_f16_f32 v2, v2, v3
	s_waitcnt lgkmcnt(2)
	v_mfma_f32_16x16x32_f16 v[30:33], v[18:21], v[14:17], v[22:25]
	v_cvt_pk_f16_f32 v3, v4, v5
	s_add_i32 s10, s20, s12
	s_nop 0
	v_mfma_f32_16x16x32_f16 v[18:21], v[18:21], v[0:3], v[22:25]
	ds_read_b128 v[4:7], v72 offset:2048
	s_nop 1
	ds_read_b128 v[22:25], v71 offset:42112
	s_waitcnt lgkmcnt(2)
	v_exp_f32_e32 v78, v30
	v_mfma_f32_16x16x32_f16 v[34:37], v[10:13], v[14:17], v[26:29]
	v_exp_f32_e32 v79, v31
	v_exp_f32_e32 v20, v20
	v_mfma_f32_16x16x32_f16 v[8:11], v[10:13], v[0:3], v[26:29]
	ds_read_b128 v[44:47], v71 offset:42176
	s_nop 3
	v_exp_f32_e64 v80, v34 clamp
	v_exp_f32_e64 v81, v35 clamp
	ds_read_b128 v[26:29], v72 offset:3072
	s_waitcnt lgkmcnt(2)
	v_mfma_f32_16x16x32_f16 v[48:51], v[4:7], v[14:17], v[22:25]
	v_exp_f32_e64 v82, v36 clamp
	v_exp_f32_e64 v83, v37 clamp
	v_exp_f32_e32 v21, v21
	v_mfma_f32_16x16x32_f16 v[22:25], v[4:7], v[0:3], v[22:25]
	ds_read_b128 v[52:55], v72 offset:4096
	ds_read_b128 v[56:59], v71 offset:42240
	s_nop 1
	v_exp_f32_e32 v4, v48
	s_waitcnt lgkmcnt(2)
	v_mfma_f32_16x16x32_f16 v[60:63], v[26:29], v[14:17], v[44:47]
	v_exp_f32_e32 v5, v49
	v_exp_f32_e32 v48, v32
	v_exp_f32_e32 v49, v33
	v_mfma_f32_16x16x32_f16 v[26:29], v[26:29], v[0:3], v[44:47]
	v_exp_f32_e32 v6, v50
	ds_read_b128 v[64:67], v71 offset:42304
	v_exp_f32_e32 v7, v51
	ds_read_b128 v[44:47], v72 offset:5120
	s_waitcnt lgkmcnt(2)
	v_mfma_f32_16x16x32_f16 v[74:77], v[52:55], v[14:17], v[56:59]
	v_exp_f32_e32 v50, v18
	v_exp_f32_e32 v51, v19
	v_exp_f32_e32 v26, v26
	v_mfma_f32_16x16x32_f16 v[30:33], v[52:55], v[0:3], v[56:59]
	v_exp_f32_e64 v52, v8 clamp
	v_exp_f32_e64 v53, v9 clamp
	v_exp_f32_e32 v8, v22
	s_waitcnt lgkmcnt(0)
	v_mfma_f32_16x16x32_f16 v[34:37], v[44:47], v[14:17], v[64:67]
	v_exp_f32_e32 v9, v23
	v_exp_f32_e64 v22, v10 clamp
	v_exp_f32_e64 v23, v11 clamp
	v_mfma_f32_16x16x32_f16 v[44:47], v[44:47], v[0:3], v[64:67]
	v_exp_f32_e32 v10, v24
	v_exp_f32_e32 v11, v25
	s_nop 1
	v_exp_f32_e32 v12, v34
	v_exp_f32_e32 v13, v35
	v_exp_f32_e32 v18, v36
	v_exp_f32_e32 v24, v60
	v_exp_f32_e32 v25, v61
	v_exp_f32_e64 v54, v74 clamp
	v_exp_f32_e64 v55, v75 clamp
	v_exp_f32_e32 v34, v62
	v_exp_f32_e32 v35, v63
	v_exp_f32_e64 v56, v76 clamp
	v_exp_f32_e64 v57, v77 clamp
	v_exp_f32_e32 v19, v37
	v_exp_f32_e32 v27, v27
	v_exp_f32_e64 v30, v30 clamp
	v_exp_f32_e64 v31, v31 clamp
	v_exp_f32_e32 v36, v44
	v_exp_f32_e32 v37, v45
	v_exp_f32_e32 v28, v28
	v_exp_f32_e32 v29, v29
	v_exp_f32_e64 v32, v32 clamp
	v_exp_f32_e64 v33, v33 clamp
	v_exp_f32_e32 v44, v46
	v_exp_f32_e32 v45, v47
	v_pk_fma_f32 v[58:59], v[80:81], s[2:3], 1.0 op_sel_hi:[1,0,0]
	v_pk_fma_f32 v[60:61], v[82:83], s[2:3], 1.0 op_sel_hi:[1,0,0]
	v_pk_fma_f32 v[52:53], v[52:53], s[2:3], 1.0 op_sel_hi:[1,0,0]
	v_pk_fma_f32 v[22:23], v[22:23], s[2:3], 1.0 op_sel_hi:[1,0,0]
	v_pk_fma_f32 v[54:55], v[54:55], s[2:3], 1.0 op_sel_hi:[1,0,0]
	v_pk_fma_f32 v[56:57], v[56:57], s[2:3], 1.0 op_sel_hi:[1,0,0]
	v_pk_fma_f32 v[30:31], v[30:31], s[2:3], 1.0 op_sel_hi:[1,0,0]
	v_pk_fma_f32 v[32:33], v[32:33], s[2:3], 1.0 op_sel_hi:[1,0,0]
	v_pk_fma_f32 v[46:47], v[78:79], v[58:59], v[58:59]
	v_pk_fma_f32 v[48:49], v[48:49], v[60:61], v[60:61]
	v_pk_fma_f32 v[50:51], v[50:51], v[52:53], v[52:53]
	v_pk_fma_f32 v[20:21], v[20:21], v[22:23], v[22:23]
	v_pk_fma_f32 v[24:25], v[24:25], v[54:55], v[54:55]
	v_pk_fma_f32 v[34:35], v[34:35], v[56:57], v[56:57]
	v_pk_fma_f32 v[26:27], v[26:27], v[30:31], v[30:31]
	v_pk_fma_f32 v[28:29], v[28:29], v[32:33], v[32:33]
	v_pk_fma_f32 v[58:59], v[58:59], s[6:7], v[40:41] op_sel_hi:[1,0,0] neg_lo:[1,0,0] neg_hi:[1,0,0]
	v_pk_fma_f32 v[60:61], v[60:61], s[6:7], v[40:41] op_sel_hi:[1,0,0] neg_lo:[1,0,0] neg_hi:[1,0,0]
	v_pk_fma_f32 v[52:53], v[52:53], s[6:7], v[40:41] op_sel_hi:[1,0,0] neg_lo:[1,0,0] neg_hi:[1,0,0]
	v_pk_fma_f32 v[22:23], v[22:23], s[6:7], v[40:41] op_sel_hi:[1,0,0] neg_lo:[1,0,0] neg_hi:[1,0,0]
	v_pk_fma_f32 v[54:55], v[54:55], s[6:7], v[40:41] op_sel_hi:[1,0,0] neg_lo:[1,0,0] neg_hi:[1,0,0]
	v_pk_fma_f32 v[56:57], v[56:57], s[6:7], v[40:41] op_sel_hi:[1,0,0] neg_lo:[1,0,0] neg_hi:[1,0,0]
	v_pk_fma_f32 v[30:31], v[30:31], s[6:7], v[40:41] op_sel_hi:[1,0,0] neg_lo:[1,0,0] neg_hi:[1,0,0]
	v_pk_fma_f32 v[32:33], v[32:33], s[6:7], v[40:41] op_sel_hi:[1,0,0] neg_lo:[1,0,0] neg_hi:[1,0,0]
	v_pk_fma_f32 v[46:47], v[4:5], v[46:47], v[46:47]
	v_pk_fma_f32 v[48:49], v[6:7], v[48:49], v[48:49]
	v_pk_fma_f32 v[50:51], v[8:9], v[50:51], v[50:51]
	v_pk_fma_f32 v[20:21], v[10:11], v[20:21], v[20:21]
	v_pk_fma_f32 v[24:25], v[12:13], v[24:25], v[24:25]
	v_pk_fma_f32 v[34:35], v[18:19], v[34:35], v[34:35]
	v_pk_fma_f32 v[26:27], v[36:37], v[26:27], v[26:27]
	v_pk_fma_f32 v[28:29], v[44:45], v[28:29], v[28:29]
	v_rcp_f32_e64 v46, v46 clamp
	v_rcp_f32_e64 v47, v47 clamp
	v_rcp_f32_e64 v48, v48 clamp
	v_rcp_f32_e64 v49, v49 clamp
	v_rcp_f32_e64 v50, v50 clamp
	v_rcp_f32_e64 v51, v51 clamp
	v_rcp_f32_e64 v20, v20 clamp
	v_rcp_f32_e64 v21, v21 clamp
	v_rcp_f32_e64 v24, v24 clamp
	v_rcp_f32_e64 v25, v25 clamp
	v_rcp_f32_e64 v34, v34 clamp
	v_rcp_f32_e64 v35, v35 clamp
	v_rcp_f32_e64 v26, v26 clamp
	v_rcp_f32_e64 v27, v27 clamp
	v_rcp_f32_e64 v28, v28 clamp
	v_rcp_f32_e64 v29, v29 clamp
	v_pk_mul_f32 v[46:47], v[58:59], v[46:47]
	v_pk_mul_f32 v[48:49], v[60:61], v[48:49]
	v_pk_mul_f32 v[50:51], v[52:53], v[50:51]
	v_pk_mul_f32 v[20:21], v[22:23], v[20:21]
	v_pk_mul_f32 v[22:23], v[54:55], v[24:25]
	v_pk_mul_f32 v[24:25], v[56:57], v[34:35]
	v_pk_mul_f32 v[26:27], v[30:31], v[26:27]
	v_pk_mul_f32 v[28:29], v[32:33], v[28:29]
	v_pk_fma_f32 v[4:5], v[4:5], v[46:47], v[46:47]
	v_pk_fma_f32 v[6:7], v[6:7], v[48:49], v[48:49]
	v_pk_fma_f32 v[8:9], v[8:9], v[50:51], v[50:51]
	v_pk_fma_f32 v[10:11], v[10:11], v[20:21], v[20:21]
	v_pk_fma_f32 v[12:13], v[12:13], v[22:23], v[22:23]
	v_pk_fma_f32 v[18:19], v[18:19], v[24:25], v[24:25]
	v_pk_fma_f32 v[30:31], v[36:37], v[26:27], v[26:27]
	v_pk_fma_f32 v[32:33], v[44:45], v[28:29], v[28:29]
	s_nop 0
	v_pk_fma_f32 v[4:5], v[4:5], v[4:5], s[4:5] neg_lo:[1,0,0] neg_hi:[1,0,0] clamp
	v_pk_fma_f32 v[6:7], v[6:7], v[6:7], s[4:5] neg_lo:[1,0,0] neg_hi:[1,0,0] clamp
	v_pk_fma_f32 v[8:9], v[8:9], v[8:9], s[4:5] neg_lo:[1,0,0] neg_hi:[1,0,0] clamp
	v_pk_fma_f32 v[10:11], v[10:11], v[10:11], s[4:5] neg_lo:[1,0,0] neg_hi:[1,0,0] clamp
	v_pk_fma_f32 v[12:13], v[12:13], v[12:13], s[4:5] neg_lo:[1,0,0] neg_hi:[1,0,0] clamp
	v_pk_fma_f32 v[18:19], v[18:19], v[18:19], s[4:5] neg_lo:[1,0,0] neg_hi:[1,0,0] clamp
	v_pk_fma_f32 v[30:31], v[30:31], v[30:31], s[4:5] neg_lo:[1,0,0] neg_hi:[1,0,0] clamp
	s_nop 0
	v_pk_fma_f32 v[32:33], v[32:33], v[32:33], s[4:5] neg_lo:[1,0,0] neg_hi:[1,0,0] clamp
	s_nop 0
	v_pk_fma_f32 v[8:9], v[8:9], v[8:9], s[8:9] op_sel_hi:[1,1,0]
	v_pk_fma_f32 v[10:11], v[10:11], v[10:11], s[8:9] op_sel_hi:[1,1,0]
	v_pk_fma_f32 v[12:13], v[12:13], v[12:13], s[8:9] op_sel_hi:[1,1,0]
	v_pk_fma_f32 v[18:19], v[18:19], v[18:19], s[8:9] op_sel_hi:[1,1,0]
	v_pk_fma_f32 v[32:33], v[32:33], v[32:33], s[8:9] op_sel_hi:[1,1,0]
	v_pk_fma_f32 v[4:5], v[4:5], v[4:5], s[8:9] op_sel_hi:[1,1,0]
	v_pk_fma_f32 v[6:7], v[6:7], v[6:7], s[8:9] op_sel_hi:[1,1,0]
	v_pk_fma_f32 v[30:31], v[30:31], v[30:31], s[8:9] op_sel_hi:[1,1,0]
	v_pk_mul_f32 v[8:9], v[50:51], v[8:9]
	v_pk_mul_f32 v[84:85], v[20:21], v[10:11]
	v_pk_mul_f32 v[86:87], v[22:23], v[12:13]
	v_pk_mul_f32 v[10:11], v[24:25], v[18:19]
	v_pk_mul_f32 v[12:13], v[28:29], v[32:33]
	v_pk_mul_f32 v[64:65], v[46:47], v[4:5]
	v_pk_mul_f32 v[82:83], v[48:49], v[6:7]
	v_pk_mul_f32 v[20:21], v[30:31], v[26:27]
	ds_read_b128 v[4:7], v72 offset:6144
	ds_read_b128 v[22:25], v71 offset:42368
	ds_read_b128 v[26:29], v72 offset:7168
	ds_read_b128 v[30:33], v71 offset:42432
	v_cvt_pk_f16_f32 v19, v84, v85
	v_cvt_pk_f16_f32 v18, v8, v9
	v_cvt_pk_f16_f32 v20, v20, v21
	s_waitcnt lgkmcnt(2)
	v_mfma_f32_16x16x32_f16 v[34:37], v[4:7], v[14:17], v[22:25]
	v_cvt_pk_f16_f32 v21, v12, v13
	v_mfma_f32_16x16x32_f16 v[44:47], v[4:7], v[0:3], v[22:25]
	ds_read_b128 v[4:7], v72 offset:8192
	ds_read_b128 v[48:51], v71 offset:42496
	s_waitcnt lgkmcnt(2)
	v_cvt_pk_f16_f32 v22, v64, v65
	v_mfma_f32_16x16x32_f16 v[52:55], v[26:29], v[14:17], v[30:33]
	v_cvt_pk_f16_f32 v23, v82, v83
	v_cvt_pk_f16_f32 v24, v86, v87
	v_mfma_f32_16x16x32_f16 v[26:29], v[26:29], v[0:3], v[30:33]
	v_exp_f32_e32 v86, v34
	ds_read_b128 v[56:59], v71 offset:42560
	v_exp_f32_e32 v87, v35
	ds_read_b128 v[30:33], v72 offset:9216
	s_waitcnt lgkmcnt(2)
	v_mfma_f32_16x16x32_f16 v[60:63], v[4:7], v[14:17], v[48:51]
	v_exp_f32_e64 v88, v52 clamp
	v_exp_f32_e64 v89, v53 clamp
	v_exp_f32_e64 v90, v54 clamp
	v_mfma_f32_16x16x32_f16 v[48:51], v[4:7], v[0:3], v[48:51]
	ds_read_b128 v[64:67], v72 offset:10240
	ds_read_b128 v[74:77], v71 offset:42624
	s_nop 1
	v_exp_f32_e32 v4, v60
	s_waitcnt lgkmcnt(2)
	v_mfma_f32_16x16x32_f16 v[78:81], v[30:33], v[14:17], v[56:59]
	v_exp_f32_e32 v5, v61
	v_exp_f32_e32 v60, v36
	v_exp_f32_e32 v61, v37
	v_mfma_f32_16x16x32_f16 v[30:33], v[30:33], v[0:3], v[56:59]
	v_exp_f32_e64 v91, v55 clamp
	ds_read_b128 v[82:85], v71 offset:42688
	v_exp_f32_e32 v6, v62
	ds_read_b128 v[56:59], v72 offset:11264
	s_waitcnt lgkmcnt(2)
	v_mfma_f32_16x16x32_f16 v[34:37], v[64:67], v[14:17], v[74:77]
	v_exp_f32_e32 v7, v63
	v_exp_f32_e32 v8, v48
	v_exp_f32_e32 v9, v49
	v_mfma_f32_16x16x32_f16 v[52:55], v[64:67], v[0:3], v[74:77]
	v_exp_f32_e32 v44, v44
	v_exp_f32_e32 v45, v45
	v_exp_f32_e64 v26, v26 clamp
	s_waitcnt lgkmcnt(0)
	v_mfma_f32_16x16x32_f16 v[14:17], v[56:59], v[14:17], v[82:85]
	v_exp_f32_e64 v27, v27 clamp
	v_exp_f32_e32 v46, v46
	v_exp_f32_e32 v47, v47
	v_mfma_f32_16x16x32_f16 v[56:59], v[56:59], v[0:3], v[82:85]
	v_exp_f32_e64 v28, v28 clamp
	s_nop 2
	v_exp_f32_e32 v2, v14
	v_exp_f32_e32 v3, v15
	v_exp_f32_e32 v14, v16
	v_exp_f32_e32 v15, v17
	v_exp_f32_e32 v16, v30
	v_exp_f32_e32 v17, v31
	v_exp_f32_e64 v29, v29 clamp
	v_exp_f32_e32 v0, v50
	v_exp_f32_e32 v1, v51
	v_exp_f32_e32 v48, v78
	v_exp_f32_e32 v49, v79
	v_exp_f32_e64 v34, v34 clamp
	v_exp_f32_e64 v35, v35 clamp
	v_exp_f32_e32 v50, v80
	v_exp_f32_e32 v51, v81
	v_exp_f32_e64 v36, v36 clamp
	v_exp_f32_e64 v37, v37 clamp
	v_exp_f32_e64 v30, v52 clamp
	v_exp_f32_e64 v31, v53 clamp
	v_exp_f32_e32 v52, v56
	v_exp_f32_e32 v53, v57
	v_exp_f32_e32 v32, v32
	v_exp_f32_e32 v33, v33
	v_exp_f32_e64 v54, v54 clamp
	v_exp_f32_e64 v55, v55 clamp
	v_exp_f32_e32 v56, v58
	v_cvt_pk_f16_f32 v25, v10, v11
	v_exp_f32_e32 v57, v59
	v_pk_fma_f32 v[30:31], v[30:31], s[2:3], 1.0 op_sel_hi:[1,0,0]
	v_pk_fma_f32 v[10:11], v[88:89], s[2:3], 1.0 op_sel_hi:[1,0,0]
	v_pk_fma_f32 v[12:13], v[90:91], s[2:3], 1.0 op_sel_hi:[1,0,0]
	v_pk_fma_f32 v[26:27], v[26:27], s[2:3], 1.0 op_sel_hi:[1,0,0]
	v_pk_fma_f32 v[28:29], v[28:29], s[2:3], 1.0 op_sel_hi:[1,0,0]
	v_pk_fma_f32 v[34:35], v[34:35], s[2:3], 1.0 op_sel_hi:[1,0,0]
	v_pk_fma_f32 v[36:37], v[36:37], s[2:3], 1.0 op_sel_hi:[1,0,0]
	v_pk_fma_f32 v[54:55], v[54:55], s[2:3], 1.0 op_sel_hi:[1,0,0]
	v_pk_fma_f32 v[16:17], v[16:17], v[30:31], v[30:31]
	v_pk_fma_f32 v[58:59], v[86:87], v[10:11], v[10:11]
	v_pk_fma_f32 v[10:11], v[10:11], s[6:7], v[40:41] op_sel_hi:[1,0,0] neg_lo:[1,0,0] neg_hi:[1,0,0]
	v_pk_fma_f32 v[60:61], v[60:61], v[12:13], v[12:13]
	v_pk_fma_f32 v[12:13], v[12:13], s[6:7], v[40:41] op_sel_hi:[1,0,0] neg_lo:[1,0,0] neg_hi:[1,0,0]
	v_pk_fma_f32 v[44:45], v[44:45], v[26:27], v[26:27]
	v_pk_fma_f32 v[46:47], v[46:47], v[28:29], v[28:29]
	v_pk_fma_f32 v[48:49], v[48:49], v[34:35], v[34:35]
	v_pk_fma_f32 v[50:51], v[50:51], v[36:37], v[36:37]
	v_pk_fma_f32 v[32:33], v[32:33], v[54:55], v[54:55]
	v_pk_fma_f32 v[16:17], v[52:53], v[16:17], v[16:17]
	v_pk_fma_f32 v[26:27], v[26:27], s[6:7], v[40:41] op_sel_hi:[1,0,0] neg_lo:[1,0,0] neg_hi:[1,0,0]
	v_pk_fma_f32 v[28:29], v[28:29], s[6:7], v[40:41] op_sel_hi:[1,0,0] neg_lo:[1,0,0] neg_hi:[1,0,0]
	v_pk_fma_f32 v[34:35], v[34:35], s[6:7], v[40:41] op_sel_hi:[1,0,0] neg_lo:[1,0,0] neg_hi:[1,0,0]
	v_pk_fma_f32 v[36:37], v[36:37], s[6:7], v[40:41] op_sel_hi:[1,0,0] neg_lo:[1,0,0] neg_hi:[1,0,0]
	v_pk_fma_f32 v[30:31], v[30:31], s[6:7], v[40:41] op_sel_hi:[1,0,0] neg_lo:[1,0,0] neg_hi:[1,0,0]
	v_pk_fma_f32 v[54:55], v[54:55], s[6:7], v[40:41] op_sel_hi:[1,0,0] neg_lo:[1,0,0] neg_hi:[1,0,0]
	v_pk_fma_f32 v[58:59], v[4:5], v[58:59], v[58:59]
	v_pk_fma_f32 v[60:61], v[6:7], v[60:61], v[60:61]
	v_pk_fma_f32 v[44:45], v[8:9], v[44:45], v[44:45]
	v_pk_fma_f32 v[46:47], v[0:1], v[46:47], v[46:47]
	v_pk_fma_f32 v[48:49], v[2:3], v[48:49], v[48:49]
	v_pk_fma_f32 v[50:51], v[14:15], v[50:51], v[50:51]
	v_pk_fma_f32 v[32:33], v[56:57], v[32:33], v[32:33]
	v_rcp_f32_e64 v16, v16 clamp
	v_rcp_f32_e64 v17, v17 clamp
	v_rcp_f32_e64 v58, v58 clamp
	v_rcp_f32_e64 v59, v59 clamp
	v_rcp_f32_e64 v60, v60 clamp
	v_rcp_f32_e64 v61, v61 clamp
	v_rcp_f32_e64 v44, v44 clamp
	v_rcp_f32_e64 v45, v45 clamp
	v_rcp_f32_e64 v46, v46 clamp
	v_rcp_f32_e64 v47, v47 clamp
	v_rcp_f32_e64 v48, v48 clamp
	v_rcp_f32_e64 v49, v49 clamp
	v_rcp_f32_e64 v50, v50 clamp
	v_rcp_f32_e64 v51, v51 clamp
	v_rcp_f32_e64 v32, v32 clamp
	v_rcp_f32_e64 v33, v33 clamp
	v_pk_mul_f32 v[10:11], v[10:11], v[58:59]
	v_pk_mul_f32 v[12:13], v[12:13], v[60:61]
	v_pk_mul_f32 v[26:27], v[26:27], v[44:45]
	v_pk_mul_f32 v[34:35], v[34:35], v[48:49]
	v_pk_mul_f32 v[36:37], v[36:37], v[50:51]
	v_pk_mul_f32 v[28:29], v[28:29], v[46:47]
	v_pk_mul_f32 v[16:17], v[30:31], v[16:17]
	v_pk_mul_f32 v[30:31], v[54:55], v[32:33]
	v_pk_fma_f32 v[4:5], v[4:5], v[10:11], v[10:11]
	v_pk_fma_f32 v[6:7], v[6:7], v[12:13], v[12:13]
	v_pk_fma_f32 v[8:9], v[8:9], v[26:27], v[26:27]
	v_pk_fma_f32 v[2:3], v[2:3], v[34:35], v[34:35]
	v_pk_fma_f32 v[14:15], v[14:15], v[36:37], v[36:37]
	v_pk_fma_f32 v[0:1], v[0:1], v[28:29], v[28:29]
	v_pk_fma_f32 v[32:33], v[52:53], v[16:17], v[16:17]
	v_pk_fma_f32 v[44:45], v[56:57], v[30:31], v[30:31]
	s_nop 0
	v_pk_fma_f32 v[4:5], v[4:5], v[4:5], s[4:5] neg_lo:[1,0,0] neg_hi:[1,0,0] clamp
	v_pk_fma_f32 v[6:7], v[6:7], v[6:7], s[4:5] neg_lo:[1,0,0] neg_hi:[1,0,0] clamp
	v_pk_fma_f32 v[8:9], v[8:9], v[8:9], s[4:5] neg_lo:[1,0,0] neg_hi:[1,0,0] clamp
	v_pk_fma_f32 v[0:1], v[0:1], v[0:1], s[4:5] neg_lo:[1,0,0] neg_hi:[1,0,0] clamp
	v_pk_fma_f32 v[2:3], v[2:3], v[2:3], s[4:5] neg_lo:[1,0,0] neg_hi:[1,0,0] clamp
	v_pk_fma_f32 v[14:15], v[14:15], v[14:15], s[4:5] neg_lo:[1,0,0] neg_hi:[1,0,0] clamp
	v_pk_fma_f32 v[32:33], v[32:33], v[32:33], s[4:5] neg_lo:[1,0,0] neg_hi:[1,0,0] clamp
	s_nop 0
	v_pk_fma_f32 v[44:45], v[44:45], v[44:45], s[4:5] neg_lo:[1,0,0] neg_hi:[1,0,0] clamp
	s_nop 0
	v_pk_fma_f32 v[32:33], v[32:33], v[32:33], s[8:9] op_sel_hi:[1,1,0]
	v_pk_fma_f32 v[4:5], v[4:5], v[4:5], s[8:9] op_sel_hi:[1,1,0]
	v_pk_fma_f32 v[6:7], v[6:7], v[6:7], s[8:9] op_sel_hi:[1,1,0]
	v_pk_fma_f32 v[8:9], v[8:9], v[8:9], s[8:9] op_sel_hi:[1,1,0]
	v_pk_fma_f32 v[0:1], v[0:1], v[0:1], s[8:9] op_sel_hi:[1,1,0]
	v_pk_fma_f32 v[2:3], v[2:3], v[2:3], s[8:9] op_sel_hi:[1,1,0]
	v_pk_fma_f32 v[14:15], v[14:15], v[14:15], s[8:9] op_sel_hi:[1,1,0]
	v_pk_fma_f32 v[44:45], v[44:45], v[44:45], s[8:9] op_sel_hi:[1,1,0]
	v_pk_mul_f32 v[16:17], v[32:33], v[16:17]
	v_pk_mul_f32 v[52:53], v[10:11], v[4:5]
	v_pk_mul_f32 v[54:55], v[12:13], v[6:7]
	v_pk_mul_f32 v[26:27], v[26:27], v[8:9]
	v_pk_mul_f32 v[28:29], v[28:29], v[0:1]
	v_pk_mul_f32 v[56:57], v[34:35], v[2:3]
	v_pk_mul_f32 v[58:59], v[36:37], v[14:15]
	v_pk_mul_f32 v[60:61], v[30:31], v[44:45]
	s_cmp_lt_u32 s33, 8
	s_cbranch_scc1 .Lprio_half
	s_setprio 0
.Lprio_half:
	ds_read_b128 v[0:3], v72 offset:12288
	ds_read_b128 v[4:7], v71 offset:42752
	ds_read_b128 v[8:11], v72 offset:13312
	ds_read_b128 v[12:15], v72 offset:14336
	ds_read_b128 v[34:37], v72 offset:15360
	ds_read_b128 v[44:47], v71 offset:42816
	v_cvt_pk_f16_f32 v30, v52, v53
	v_cvt_pk_f16_f32 v26, v26, v27
	v_cvt_pk_f16_f32 v31, v54, v55
	s_waitcnt lgkmcnt(4)
	v_mfma_f32_16x16x32_f16 v[48:51], v[0:3], v[22:25], v[4:7]
	v_cvt_pk_f16_f32 v32, v56, v57
	v_cvt_pk_f16_f32 v33, v58, v59
	v_cvt_pk_f16_f32 v27, v28, v29
	v_mfma_f32_16x16x32_f16 v[0:3], v[0:3], v[18:21], v[4:7]
	v_cvt_pk_f16_f32 v28, v16, v17
	s_add_i32 s11, s9, s12
	s_waitcnt lgkmcnt(3)
	v_mfma_f32_16x16x32_f16 v[48:51], v[8:11], v[30:33], v[48:51]
	v_cvt_pk_f16_f32 v29, v60, v61
	s_cmp_lt_i32 s11, 0x8000
	s_cselect_b32 s10, s11, s10
	s_ashr_i32 s11, s10, 31
	v_mfma_f32_16x16x32_f16 v[52:55], v[8:11], v[26:29], v[0:3]
	ds_read_b128 v[4:7], v72 offset:17408
	ds_read_b128 v[8:11], v71 offset:42880
	s_lshl_b64 s[10:11], s[10:11], 12
	s_add_u32 s10, s10, s36
	s_addc_u32 s11, s11, s37
	ds_read_b128 v[0:3], v72 offset:16384
	s_waitcnt lgkmcnt(3)
	v_exp_f32_e32 v106, v48
	v_mfma_f32_16x16x32_f16 v[56:59], v[12:15], v[22:25], v[44:47]
	v_exp_f32_e32 v107, v49
	v_exp_f32_e32 v110, v50
	v_mfma_f32_16x16x32_f16 v[12:15], v[12:15], v[18:21], v[44:47]
	v_exp_f32_e32 v111, v51
	v_exp_f32_e32 v114, v52
	v_mfma_f32_16x16x32_f16 v[44:47], v[34:37], v[30:33], v[56:59]
	v_exp_f32_e32 v115, v53
	v_mfma_f32_16x16x32_f16 v[56:59], v[34:37], v[26:29], v[12:15]
	ds_read_b128 v[34:37], v72 offset:19456
	ds_read_b128 v[60:63], v71 offset:42944
	s_nop 4
	v_exp_f32_e64 v108, v44 clamp
	ds_read_b128 v[12:15], v72 offset:18432
	s_waitcnt lgkmcnt(3)
	v_mfma_f32_16x16x32_f16 v[64:67], v[0:3], v[22:25], v[8:11]
	v_exp_f32_e64 v109, v45 clamp
	v_mfma_f32_16x16x32_f16 v[0:3], v[0:3], v[18:21], v[8:11]
	v_exp_f32_e64 v116, v56 clamp
	v_mfma_f32_16x16x32_f16 v[64:67], v[4:7], v[30:33], v[64:67]
	v_exp_f32_e64 v59, v59 clamp
	v_mfma_f32_16x16x32_f16 v[74:77], v[4:7], v[26:29], v[0:3]
	v_exp_f32_e64 v58, v58 clamp
	ds_read_b128 v[78:81], v72 offset:20480
	ds_read_b128 v[82:85], v72 offset:21504
	ds_read_b128 v[86:89], v71 offset:43008
	s_waitcnt lgkmcnt(3)
	v_mfma_f32_16x16x32_f16 v[6:9], v[12:15], v[22:25], v[60:63]
	v_exp_f32_e64 v117, v57 clamp
	v_mfma_f32_16x16x32_f16 v[60:63], v[12:15], v[18:21], v[60:63]
	v_exp_f32_e64 v113, v47 clamp
	global_load_dwordx4 v[10:13], v39, s[10:11] offset:16
	global_load_dwordx4 v[14:17], v39, s[10:11]
	global_load_dwordx4 v[2:5], v39, s[10:11] offset:2064
	v_mfma_f32_16x16x32_f16 v[90:93], v[34:37], v[30:33], v[6:9]
	v_exp_f32_e64 v112, v46 clamp
	v_mfma_f32_16x16x32_f16 v[60:63], v[34:37], v[26:29], v[60:63]
	s_nop 1
	global_load_dwordx4 v[6:9], v39, s[10:11] offset:2048
	ds_read_b128 v[94:97], v72 offset:22528
	ds_read_b128 v[98:101], v72 offset:23552
	ds_read_b128 v[102:105], v71 offset:43072
	s_waitcnt lgkmcnt(3)
	v_exp_f32_e32 v0, v64
	v_mfma_f32_16x16x32_f16 v[44:47], v[78:81], v[22:25], v[86:89]
	v_exp_f32_e32 v1, v65
	v_exp_f32_e32 v34, v66
	v_mfma_f32_16x16x32_f16 v[48:51], v[78:81], v[18:21], v[86:89]
	v_exp_f32_e32 v35, v67
	v_exp_f32_e32 v36, v74
	v_exp_f32_e32 v37, v75
	v_mfma_f32_16x16x32_f16 v[64:67], v[82:85], v[30:33], v[44:47]
	v_exp_f32_e32 v74, v54
	v_exp_f32_e32 v75, v55
	v_exp_f32_e32 v78, v92
	v_mfma_f32_16x16x32_f16 v[50:53], v[82:85], v[26:29], v[48:51]
	v_exp_f32_e32 v44, v76
	v_exp_f32_e32 v45, v77
	v_exp_f32_e32 v76, v90
	s_waitcnt lgkmcnt(0)
	v_mfma_f32_16x16x32_f16 v[46:49], v[94:97], v[22:25], v[102:105]
	v_exp_f32_e32 v77, v91
	v_exp_f32_e64 v64, v64 clamp
	v_exp_f32_e64 v65, v65 clamp
	v_mfma_f32_16x16x32_f16 v[54:57], v[94:97], v[18:21], v[102:105]
	v_exp_f32_e32 v79, v93
	v_exp_f32_e64 v66, v66 clamp
	v_exp_f32_e64 v67, v67 clamp
	v_mfma_f32_16x16x32_f16 v[46:49], v[98:101], v[30:33], v[46:49]
	v_exp_f32_e32 v60, v60
	v_exp_f32_e32 v61, v61
	v_exp_f32_e64 v50, v50 clamp
	v_mfma_f32_16x16x32_f16 v[54:57], v[98:101], v[26:29], v[54:57]
	v_exp_f32_e64 v51, v51 clamp
	s_nop 2
	v_exp_f32_e32 v46, v46
	v_exp_f32_e32 v47, v47
	v_exp_f32_e32 v48, v48
	v_exp_f32_e32 v49, v49
	v_exp_f32_e32 v54, v54
	v_exp_f32_e32 v55, v55
	v_exp_f32_e32 v62, v62
	v_exp_f32_e32 v63, v63
	v_exp_f32_e64 v52, v52 clamp
	v_exp_f32_e64 v53, v53 clamp
	v_exp_f32_e32 v56, v56
	v_exp_f32_e32 v57, v57
	v_pk_fma_f32 v[80:81], v[108:109], s[2:3], 1.0 op_sel_hi:[1,0,0]
	v_pk_fma_f32 v[82:83], v[112:113], s[2:3], 1.0 op_sel_hi:[1,0,0]
	v_pk_fma_f32 v[84:85], v[116:117], s[2:3], 1.0 op_sel_hi:[1,0,0]
	v_pk_fma_f32 v[58:59], v[58:59], s[2:3], 1.0 op_sel_hi:[1,0,0]
	v_pk_fma_f32 v[64:65], v[64:65], s[2:3], 1.0 op_sel_hi:[1,0,0]
	v_pk_fma_f32 v[66:67], v[66:67], s[2:3], 1.0 op_sel_hi:[1,0,0]
	v_pk_fma_f32 v[50:51], v[50:51], s[2:3], 1.0 op_sel_hi:[1,0,0]
	v_pk_fma_f32 v[52:53], v[52:53], s[2:3], 1.0 op_sel_hi:[1,0,0]
	v_pk_fma_f32 v[86:87], v[106:107], v[80:81], v[80:81]
	v_pk_fma_f32 v[88:89], v[110:111], v[82:83], v[82:83]
	v_pk_fma_f32 v[90:91], v[114:115], v[84:85], v[84:85]
	v_pk_fma_f32 v[74:75], v[74:75], v[58:59], v[58:59]
	v_pk_fma_f32 v[76:77], v[76:77], v[64:65], v[64:65]
	v_pk_fma_f32 v[78:79], v[78:79], v[66:67], v[66:67]
	v_pk_fma_f32 v[60:61], v[60:61], v[50:51], v[50:51]
	v_pk_fma_f32 v[62:63], v[62:63], v[52:53], v[52:53]
	v_pk_fma_f32 v[80:81], v[80:81], s[6:7], v[40:41] op_sel_hi:[1,0,0] neg_lo:[1,0,0] neg_hi:[1,0,0]
	v_pk_fma_f32 v[82:83], v[82:83], s[6:7], v[40:41] op_sel_hi:[1,0,0] neg_lo:[1,0,0] neg_hi:[1,0,0]
	v_pk_fma_f32 v[84:85], v[84:85], s[6:7], v[40:41] op_sel_hi:[1,0,0] neg_lo:[1,0,0] neg_hi:[1,0,0]
	v_pk_fma_f32 v[58:59], v[58:59], s[6:7], v[40:41] op_sel_hi:[1,0,0] neg_lo:[1,0,0] neg_hi:[1,0,0]
	v_pk_fma_f32 v[64:65], v[64:65], s[6:7], v[40:41] op_sel_hi:[1,0,0] neg_lo:[1,0,0] neg_hi:[1,0,0]
	v_pk_fma_f32 v[66:67], v[66:67], s[6:7], v[40:41] op_sel_hi:[1,0,0] neg_lo:[1,0,0] neg_hi:[1,0,0]
	v_pk_fma_f32 v[50:51], v[50:51], s[6:7], v[40:41] op_sel_hi:[1,0,0] neg_lo:[1,0,0] neg_hi:[1,0,0]
	v_pk_fma_f32 v[52:53], v[52:53], s[6:7], v[40:41] op_sel_hi:[1,0,0] neg_lo:[1,0,0] neg_hi:[1,0,0]
	v_pk_fma_f32 v[86:87], v[0:1], v[86:87], v[86:87]
	v_pk_fma_f32 v[88:89], v[34:35], v[88:89], v[88:89]
	v_pk_fma_f32 v[90:91], v[36:37], v[90:91], v[90:91]
	v_pk_fma_f32 v[74:75], v[44:45], v[74:75], v[74:75]
	v_pk_fma_f32 v[76:77], v[46:47], v[76:77], v[76:77]
	v_pk_fma_f32 v[78:79], v[48:49], v[78:79], v[78:79]
	v_pk_fma_f32 v[60:61], v[54:55], v[60:61], v[60:61]
	v_pk_fma_f32 v[62:63], v[56:57], v[62:63], v[62:63]
	v_rcp_f32_e64 v86, v86 clamp
	v_rcp_f32_e64 v87, v87 clamp
	v_rcp_f32_e64 v88, v88 clamp
	v_rcp_f32_e64 v89, v89 clamp
	v_rcp_f32_e64 v90, v90 clamp
	v_rcp_f32_e64 v91, v91 clamp
	v_rcp_f32_e64 v74, v74 clamp
	v_rcp_f32_e64 v75, v75 clamp
	v_rcp_f32_e64 v76, v76 clamp
	v_rcp_f32_e64 v77, v77 clamp
	v_rcp_f32_e64 v78, v78 clamp
	v_rcp_f32_e64 v79, v79 clamp
	v_rcp_f32_e64 v60, v60 clamp
	v_rcp_f32_e64 v61, v61 clamp
	v_rcp_f32_e64 v62, v62 clamp
	v_rcp_f32_e64 v63, v63 clamp
	v_pk_mul_f32 v[80:81], v[80:81], v[86:87]
	v_pk_mul_f32 v[82:83], v[82:83], v[88:89]
	v_pk_mul_f32 v[84:85], v[84:85], v[90:91]
	v_pk_mul_f32 v[58:59], v[58:59], v[74:75]
	v_pk_mul_f32 v[64:65], v[64:65], v[76:77]
	v_pk_mul_f32 v[66:67], v[66:67], v[78:79]
	v_pk_mul_f32 v[50:51], v[50:51], v[60:61]
	v_pk_mul_f32 v[60:61], v[52:53], v[62:63]
	v_pk_fma_f32 v[0:1], v[0:1], v[80:81], v[80:81]
	v_pk_fma_f32 v[34:35], v[34:35], v[82:83], v[82:83]
	v_pk_fma_f32 v[36:37], v[36:37], v[84:85], v[84:85]
	v_pk_fma_f32 v[44:45], v[44:45], v[58:59], v[58:59]
	v_pk_fma_f32 v[46:47], v[46:47], v[64:65], v[64:65]
	v_pk_fma_f32 v[48:49], v[48:49], v[66:67], v[66:67]
	v_pk_fma_f32 v[52:53], v[54:55], v[50:51], v[50:51]
	v_pk_fma_f32 v[54:55], v[56:57], v[60:61], v[60:61]
	s_nop 0
	v_pk_fma_f32 v[0:1], v[0:1], v[0:1], s[4:5] neg_lo:[1,0,0] neg_hi:[1,0,0] clamp
	v_pk_fma_f32 v[34:35], v[34:35], v[34:35], s[4:5] neg_lo:[1,0,0] neg_hi:[1,0,0] clamp
	v_pk_fma_f32 v[36:37], v[36:37], v[36:37], s[4:5] neg_lo:[1,0,0] neg_hi:[1,0,0] clamp
	v_pk_fma_f32 v[44:45], v[44:45], v[44:45], s[4:5] neg_lo:[1,0,0] neg_hi:[1,0,0] clamp
	v_pk_fma_f32 v[46:47], v[46:47], v[46:47], s[4:5] neg_lo:[1,0,0] neg_hi:[1,0,0] clamp
	v_pk_fma_f32 v[48:49], v[48:49], v[48:49], s[4:5] neg_lo:[1,0,0] neg_hi:[1,0,0] clamp
	v_pk_fma_f32 v[52:53], v[52:53], v[52:53], s[4:5] neg_lo:[1,0,0] neg_hi:[1,0,0] clamp
	s_nop 0
	v_pk_fma_f32 v[54:55], v[54:55], v[54:55], s[4:5] neg_lo:[1,0,0] neg_hi:[1,0,0] clamp
	s_nop 0
	v_pk_fma_f32 v[0:1], v[0:1], v[0:1], s[8:9] op_sel_hi:[1,1,0]
	v_pk_fma_f32 v[56:57], v[34:35], v[34:35], s[8:9] op_sel_hi:[1,1,0]
	v_pk_fma_f32 v[36:37], v[36:37], v[36:37], s[8:9] op_sel_hi:[1,1,0]
	v_pk_fma_f32 v[44:45], v[44:45], v[44:45], s[8:9] op_sel_hi:[1,1,0]
	v_pk_fma_f32 v[46:47], v[46:47], v[46:47], s[8:9] op_sel_hi:[1,1,0]
	v_pk_fma_f32 v[48:49], v[48:49], v[48:49], s[8:9] op_sel_hi:[1,1,0]
	v_pk_fma_f32 v[62:63], v[52:53], v[52:53], s[8:9] op_sel_hi:[1,1,0]
	v_pk_fma_f32 v[74:75], v[54:55], v[54:55], s[8:9] op_sel_hi:[1,1,0]
	v_pk_mul_f32 v[34:35], v[80:81], v[0:1]
	v_pk_mul_f32 v[56:57], v[82:83], v[56:57]
	v_pk_mul_f32 v[36:37], v[84:85], v[36:37]
	v_pk_mul_f32 v[52:53], v[58:59], v[44:45]
	v_pk_mul_f32 v[54:55], v[64:65], v[46:47]
	v_pk_mul_f32 v[0:1], v[66:67], v[48:49]
	v_pk_mul_f32 v[46:47], v[62:63], v[50:51]
	v_pk_mul_f32 v[44:45], v[60:61], v[74:75]
	ds_read_b128 v[48:51], v72 offset:24576
	ds_read_b128 v[58:61], v71 offset:43136
	ds_read_b128 v[62:65], v72 offset:25600
	ds_read_b128 v[74:77], v72 offset:26624
	ds_read_b128 v[78:81], v72 offset:27648
	ds_read_b128 v[82:85], v71 offset:43200
	v_cvt_pk_f16_f32 v34, v34, v35
	s_waitcnt lgkmcnt(4)
	v_mfma_f32_16x16x32_f16 v[86:89], v[48:51], v[22:25], v[58:61]
	v_cvt_pk_f16_f32 v35, v56, v57
	v_mfma_f32_16x16x32_f16 v[48:51], v[48:51], v[18:21], v[58:61]
	s_waitcnt lgkmcnt(3)
	v_mfma_f32_16x16x32_f16 v[58:61], v[62:65], v[30:33], v[86:89]
	v_mfma_f32_16x16x32_f16 v[86:89], v[62:65], v[26:29], v[48:51]
	ds_read_b128 v[62:65], v72 offset:29696
	ds_read_b128 v[90:93], v71 offset:43264
	s_nop 2
	ds_read_b128 v[48:51], v72 offset:28672
	s_waitcnt lgkmcnt(3)
	v_mfma_f32_16x16x32_f16 v[94:97], v[74:77], v[22:25], v[82:85]
	v_exp_f32_e32 v120, v86
	v_mfma_f32_16x16x32_f16 v[74:77], v[74:77], v[18:21], v[82:85]
	v_exp_f32_e32 v123, v89
	v_mfma_f32_16x16x32_f16 v[82:85], v[78:81], v[30:33], v[94:97]
	v_exp_f32_e32 v122, v88
	v_mfma_f32_16x16x32_f16 v[74:77], v[78:81], v[26:29], v[74:77]
	v_exp_f32_e32 v121, v87
	ds_read_b128 v[78:81], v72 offset:30720
	s_nop 0
	ds_read_b128 v[94:97], v72 offset:31744
	ds_read_b128 v[98:101], v71 offset:43328
	s_waitcnt lgkmcnt(3)
	v_mfma_f32_16x16x32_f16 v[102:105], v[48:51], v[22:25], v[90:93]
	v_exp_f32_e64 v66, v82 clamp
	s_nop 0
	v_exp_f32_e64 v67, v83 clamp
	v_exp_f32_e64 v118, v84 clamp
	v_mfma_f32_16x16x32_f16 v[48:51], v[48:51], v[18:21], v[90:93]
	v_exp_f32_e64 v119, v85 clamp
	v_exp_f32_e64 v124, v74 clamp
	v_exp_f32_e64 v125, v75 clamp
	v_mfma_f32_16x16x32_f16 v[90:93], v[62:65], v[30:33], v[102:105]
	v_exp_f32_e64 v126, v76 clamp
	v_exp_f32_e64 v127, v77 clamp
	v_mfma_f32_16x16x32_f16 v[102:105], v[62:65], v[26:29], v[48:51]
	v_exp_f32_e32 v62, v58
	ds_read_b128 v[106:109], v72 offset:32768
	ds_read_b128 v[110:113], v72 offset:33792
	v_exp_f32_e32 v63, v59
	v_exp_f32_e32 v64, v60
	v_exp_f32_e32 v65, v61
	ds_read_b128 v[114:117], v71 offset:43392
	s_waitcnt lgkmcnt(3)
	v_mfma_f32_16x16x32_f16 v[58:61], v[78:81], v[22:25], v[98:101]
	v_exp_f32_e32 v48, v90
	v_exp_f32_e32 v49, v91
	v_mfma_f32_16x16x32_f16 v[78:81], v[78:81], v[18:21], v[98:101]
	v_exp_f32_e32 v51, v93
	v_mfma_f32_16x16x32_f16 v[82:85], v[94:97], v[30:33], v[58:61]
	v_exp_f32_e32 v50, v92
	v_mfma_f32_16x16x32_f16 v[78:81], v[94:97], v[26:29], v[78:81]
	ds_read_b128 v[86:89], v72 offset:34816
	ds_read_b128 v[90:93], v72 offset:35840
	ds_read_b128 v[94:97], v71 offset:43456
	s_waitcnt lgkmcnt(3)
	v_exp_f32_e32 v58, v102
	v_mfma_f32_16x16x32_f16 v[74:77], v[106:109], v[22:25], v[114:117]
	v_exp_f32_e32 v59, v103
	v_exp_f32_e32 v60, v104
	v_mfma_f32_16x16x32_f16 v[98:101], v[106:109], v[18:21], v[114:117]
	v_exp_f32_e32 v61, v105
	v_exp_f32_e32 v102, v82
	v_exp_f32_e32 v103, v83
	v_exp_f32_e32 v104, v84
	v_mfma_f32_16x16x32_f16 v[74:77], v[110:113], v[30:33], v[74:77]
	v_exp_f32_e32 v105, v85
	v_mfma_f32_16x16x32_f16 v[82:85], v[110:113], v[26:29], v[98:101]
	s_waitcnt lgkmcnt(0)
	v_mfma_f32_16x16x32_f16 v[18:21], v[86:89], v[18:21], v[94:97]
	s_nop 4
	v_exp_f32_e64 v106, v74 clamp
	v_exp_f32_e64 v107, v75 clamp
	v_exp_f32_e64 v108, v76 clamp
	v_exp_f32_e64 v109, v77 clamp
	v_mfma_f32_16x16x32_f16 v[74:77], v[86:89], v[22:25], v[94:97]
	v_cvt_pk_f16_f32 v22, v36, v37
	v_cvt_pk_f16_f32 v23, v52, v53
	v_cvt_pk_f16_f32 v36, v54, v55
	v_mfma_f32_16x16x32_f16 v[18:21], v[90:93], v[26:29], v[18:21]
	v_exp_f32_e32 v52, v78
	v_exp_f32_e32 v53, v79
	v_exp_f32_e64 v54, v82 clamp
	v_mfma_f32_16x16x32_f16 v[30:33], v[90:93], v[30:33], v[74:77]
	v_exp_f32_e64 v55, v83 clamp
	s_nop 2
	v_exp_f32_e32 v18, v18
	v_exp_f32_e32 v19, v19
	v_exp_f32_e32 v26, v80
	v_exp_f32_e32 v27, v81
	v_exp_f32_e32 v30, v30
	v_exp_f32_e32 v31, v31
	v_exp_f32_e32 v32, v32
	v_exp_f32_e32 v33, v33
	v_exp_f32_e64 v28, v84 clamp
	v_exp_f32_e64 v29, v85 clamp
	v_exp_f32_e32 v20, v20
	v_cvt_pk_f16_f32 v24, v46, v47
	v_cvt_pk_f16_f32 v37, v0, v1
	v_cvt_pk_f16_f32 v25, v44, v45
	v_exp_f32_e32 v21, v21
	v_pk_fma_f32 v[0:1], v[66:67], s[2:3], 1.0 op_sel_hi:[1,0,0]
	v_pk_fma_f32 v[44:45], v[118:119], s[2:3], 1.0 op_sel_hi:[1,0,0]
	v_pk_fma_f32 v[46:47], v[124:125], s[2:3], 1.0 op_sel_hi:[1,0,0]
	v_pk_fma_f32 v[56:57], v[126:127], s[2:3], 1.0 op_sel_hi:[1,0,0]
	v_pk_fma_f32 v[66:67], v[106:107], s[2:3], 1.0 op_sel_hi:[1,0,0]
	v_pk_fma_f32 v[74:75], v[108:109], s[2:3], 1.0 op_sel_hi:[1,0,0]
	v_pk_fma_f32 v[54:55], v[54:55], s[2:3], 1.0 op_sel_hi:[1,0,0]
	v_pk_fma_f32 v[28:29], v[28:29], s[2:3], 1.0 op_sel_hi:[1,0,0]
	v_pk_fma_f32 v[62:63], v[62:63], v[0:1], v[0:1]
	v_pk_fma_f32 v[64:65], v[64:65], v[44:45], v[44:45]
	v_pk_fma_f32 v[76:77], v[120:121], v[46:47], v[46:47]
	v_pk_fma_f32 v[78:79], v[122:123], v[56:57], v[56:57]
	v_pk_fma_f32 v[80:81], v[102:103], v[66:67], v[66:67]
	v_pk_fma_f32 v[82:83], v[104:105], v[74:75], v[74:75]
	v_pk_fma_f32 v[52:53], v[52:53], v[54:55], v[54:55]
	v_pk_fma_f32 v[26:27], v[26:27], v[28:29], v[28:29]
	v_pk_fma_f32 v[0:1], v[0:1], s[6:7], v[40:41] op_sel_hi:[1,0,0] neg_lo:[1,0,0] neg_hi:[1,0,0]
	v_pk_fma_f32 v[44:45], v[44:45], s[6:7], v[40:41] op_sel_hi:[1,0,0] neg_lo:[1,0,0] neg_hi:[1,0,0]
	v_pk_fma_f32 v[46:47], v[46:47], s[6:7], v[40:41] op_sel_hi:[1,0,0] neg_lo:[1,0,0] neg_hi:[1,0,0]
	v_pk_fma_f32 v[56:57], v[56:57], s[6:7], v[40:41] op_sel_hi:[1,0,0] neg_lo:[1,0,0] neg_hi:[1,0,0]
	v_pk_fma_f32 v[66:67], v[66:67], s[6:7], v[40:41] op_sel_hi:[1,0,0] neg_lo:[1,0,0] neg_hi:[1,0,0]
	v_pk_fma_f32 v[74:75], v[74:75], s[6:7], v[40:41] op_sel_hi:[1,0,0] neg_lo:[1,0,0] neg_hi:[1,0,0]
	v_pk_fma_f32 v[54:55], v[54:55], s[6:7], v[40:41] op_sel_hi:[1,0,0] neg_lo:[1,0,0] neg_hi:[1,0,0]
	v_pk_fma_f32 v[28:29], v[28:29], s[6:7], v[40:41] op_sel_hi:[1,0,0] neg_lo:[1,0,0] neg_hi:[1,0,0]
	v_pk_fma_f32 v[62:63], v[48:49], v[62:63], v[62:63]
	v_pk_fma_f32 v[64:65], v[50:51], v[64:65], v[64:65]
	v_pk_fma_f32 v[76:77], v[58:59], v[76:77], v[76:77]
	v_pk_fma_f32 v[78:79], v[60:61], v[78:79], v[78:79]
	v_pk_fma_f32 v[80:81], v[30:31], v[80:81], v[80:81]
	v_pk_fma_f32 v[82:83], v[32:33], v[82:83], v[82:83]
	v_pk_fma_f32 v[52:53], v[18:19], v[52:53], v[52:53]
	v_pk_fma_f32 v[26:27], v[20:21], v[26:27], v[26:27]
	v_rcp_f32_e64 v62, v62 clamp
	v_rcp_f32_e64 v63, v63 clamp
	v_rcp_f32_e64 v64, v64 clamp
	v_rcp_f32_e64 v65, v65 clamp
	v_rcp_f32_e64 v76, v76 clamp
	v_rcp_f32_e64 v77, v77 clamp
	v_rcp_f32_e64 v78, v78 clamp
	v_rcp_f32_e64 v79, v79 clamp
	v_rcp_f32_e64 v80, v80 clamp
	v_rcp_f32_e64 v81, v81 clamp
	v_rcp_f32_e64 v82, v82 clamp
	v_rcp_f32_e64 v83, v83 clamp
	v_rcp_f32_e64 v52, v52 clamp
	v_rcp_f32_e64 v53, v53 clamp
	v_rcp_f32_e64 v26, v26 clamp
	v_rcp_f32_e64 v27, v27 clamp
	v_pk_mul_f32 v[52:53], v[54:55], v[52:53]
	v_pk_mul_f32 v[0:1], v[0:1], v[62:63]
	v_pk_mul_f32 v[44:45], v[44:45], v[64:65]
	v_pk_mul_f32 v[46:47], v[46:47], v[76:77]
	v_pk_mul_f32 v[56:57], v[56:57], v[78:79]
	v_pk_mul_f32 v[62:63], v[66:67], v[80:81]
	v_pk_mul_f32 v[64:65], v[74:75], v[82:83]
	v_pk_mul_f32 v[26:27], v[28:29], v[26:27]
	v_pk_fma_f32 v[18:19], v[18:19], v[52:53], v[52:53]
	v_pk_fma_f32 v[28:29], v[48:49], v[0:1], v[0:1]
	v_pk_fma_f32 v[48:49], v[50:51], v[44:45], v[44:45]
	v_pk_fma_f32 v[50:51], v[58:59], v[46:47], v[46:47]
	v_pk_fma_f32 v[54:55], v[60:61], v[56:57], v[56:57]
	v_pk_fma_f32 v[30:31], v[30:31], v[62:63], v[62:63]
	v_pk_fma_f32 v[32:33], v[32:33], v[64:65], v[64:65]
	v_pk_fma_f32 v[20:21], v[20:21], v[26:27], v[26:27]
	s_nop 0
	v_pk_fma_f32 v[28:29], v[28:29], v[28:29], s[4:5] neg_lo:[1,0,0] neg_hi:[1,0,0] clamp
	v_pk_fma_f32 v[48:49], v[48:49], v[48:49], s[4:5] neg_lo:[1,0,0] neg_hi:[1,0,0] clamp
	v_pk_fma_f32 v[50:51], v[50:51], v[50:51], s[4:5] neg_lo:[1,0,0] neg_hi:[1,0,0] clamp
	v_pk_fma_f32 v[54:55], v[54:55], v[54:55], s[4:5] neg_lo:[1,0,0] neg_hi:[1,0,0] clamp
	v_pk_fma_f32 v[30:31], v[30:31], v[30:31], s[4:5] neg_lo:[1,0,0] neg_hi:[1,0,0] clamp
	v_pk_fma_f32 v[32:33], v[32:33], v[32:33], s[4:5] neg_lo:[1,0,0] neg_hi:[1,0,0] clamp
	v_pk_fma_f32 v[18:19], v[18:19], v[18:19], s[4:5] neg_lo:[1,0,0] neg_hi:[1,0,0] clamp
	s_nop 0
	v_pk_fma_f32 v[20:21], v[20:21], v[20:21], s[4:5] neg_lo:[1,0,0] neg_hi:[1,0,0] clamp
	s_nop 0
	v_pk_fma_f32 v[28:29], v[28:29], v[28:29], s[8:9] op_sel_hi:[1,1,0]
	v_pk_fma_f32 v[48:49], v[48:49], v[48:49], s[8:9] op_sel_hi:[1,1,0]
	v_pk_fma_f32 v[50:51], v[50:51], v[50:51], s[8:9] op_sel_hi:[1,1,0]
	v_pk_fma_f32 v[54:55], v[54:55], v[54:55], s[8:9] op_sel_hi:[1,1,0]
	v_pk_fma_f32 v[30:31], v[30:31], v[30:31], s[8:9] op_sel_hi:[1,1,0]
	v_pk_fma_f32 v[32:33], v[32:33], v[32:33], s[8:9] op_sel_hi:[1,1,0]
	v_pk_fma_f32 v[18:19], v[18:19], v[18:19], s[8:9] op_sel_hi:[1,1,0]
	v_pk_fma_f32 v[20:21], v[20:21], v[20:21], s[8:9] op_sel_hi:[1,1,0]
	v_pk_mul_f32 v[0:1], v[0:1], v[28:29]
	v_pk_mul_f32 v[58:59], v[44:45], v[48:49]
	v_pk_mul_f32 v[60:61], v[46:47], v[50:51]
	v_pk_mul_f32 v[54:55], v[56:57], v[54:55]
	v_pk_mul_f32 v[62:63], v[62:63], v[30:31]
	v_pk_mul_f32 v[64:65], v[64:65], v[32:33]
	v_pk_mul_f32 v[66:67], v[18:19], v[52:53]
	v_pk_mul_f32 v[74:75], v[26:27], v[20:21]
	ds_read_b128 v[18:21], v72 offset:36864
	ds_read_b128 v[30:33], v72 offset:37888
	ds_read_b128 v[26:29], v71 offset:43520
	v_cvt_pk_f16_f32 v56, v60, v61
	v_cvt_pk_f16_f32 v57, v54, v55
	v_cvt_pk_f16_f32 v54, v62, v63
	ds_read_b128 v[60:63], v71 offset:43584
	v_cvt_pk_f16_f32 v52, v0, v1
	v_cvt_pk_f16_f32 v53, v58, v59
	s_waitcnt lgkmcnt(1)
	v_mfma_f32_16x16x32_f16 v[48:51], v[18:21], v[34:37], v[26:29]
	v_cvt_pk_f16_f32 v55, v64, v65
	v_cvt_pk_f16_f32 v58, v66, v67
	v_mfma_f32_16x16x32_f16 v[18:21], v[18:21], v[22:25], v[26:29]
	v_cvt_pk_f16_f32 v59, v74, v75
	ds_read_b128 v[44:47], v72 offset:40960
	s_add_i32 s12, s12, s3
	s_add_i32 s10, s20, s12
	v_mfma_f32_16x16x32_f16 v[26:29], v[30:33], v[52:55], v[48:51]
	v_add_u32_e32 v38, s7, v38
	s_cmp_lt_i32 s10, 0x8000
	s_nop 0
	ds_read_b128 v[48:51], v72 offset:38912
	v_mfma_f32_16x16x32_f16 v[18:21], v[30:33], v[56:59], v[18:21]
	ds_read_b128 v[30:33], v72 offset:39936
	s_nop 1
	v_cvt_pk_f16_f32 v1, v28, v29
	v_cvt_pk_f16_f32 v0, v26, v27
	s_waitcnt lgkmcnt(1)
	v_mfma_f32_16x16x32_f16 v[34:37], v[48:51], v[34:37], v[60:63]
	v_pk_max_f16 v27, v1, 0
	v_cvt_pk_f16_f32 v1, v20, v21
	v_pk_max_f16 v26, v0, 0
	v_mfma_f32_16x16x32_f16 v[20:23], v[48:51], v[22:25], v[60:63]
	v_cvt_pk_f16_f32 v0, v18, v19
	v_pk_max_f16 v18, v0, 0
	s_waitcnt lgkmcnt(0)
	v_mfma_f32_16x16x32_f16 v[34:37], v[30:33], v[52:55], v[34:37]
	v_pk_max_f16 v19, v1, 0
	v_mfma_f32_16x16x32_f16 v[20:23], v[30:33], v[56:59], v[20:23]
	s_nop 6
	v_cvt_pk_f16_f32 v0, v34, v35
	v_cvt_pk_f16_f32 v1, v36, v37
	v_pk_max_f16 v28, v0, 0
	v_pk_max_f16 v29, v1, 0
	v_cvt_pk_f16_f32 v0, v20, v21
	v_cvt_pk_f16_f32 v1, v22, v23
	v_pk_max_f16 v20, v0, 0
	v_mfma_f32_16x16x32_f16 v[24:27], v[44:47], v[26:29], 0
	v_pk_max_f16 v21, v1, 0
	s_nop 1
	v_mfma_f32_16x16x32_f16 v[18:21], v[44:47], v[18:21], 0
	s_nop 7
	v_cndmask_b32_e64 v18, v24, v18, s[0:1]
	s_cbranch_scc0 .LBB0_37
